# first-layer out-projection epilogue: f32 residual loads of each odd 8-value group issued with the preceding even group's (two spare quads), eight exposed round trips instead of sixteen
# speedup vs baseline: 1.0102x; 1.0057x over previous
;     __device__ __forceinline__ void operator()(const Acc& acc, const Unit& u, int wr, int wc, int fr, int fq, const LAS float* tab) const {
;     ...
;                 const size_t row = (size_t)u.pm * BM + ai * HALF + wr * 64 + m * 16 + fr; const size_t off = row * D + col0; float ss = 0.f;
; #pragma unroll
;                 for (int bj = 0; bj < 2; ++bj) { f32x4 b0, b1;
;                     if (base32) { b0 = __builtin_nontemporal_load((const f32x4*)(base32 + off + bj * HALF)); b1 = __builtin_nontemporal_load((const f32x4*)(base32 + off + bj * HALF + 4)); }
;                     else { const u32x4 b4 = rb[ai][m][bj];
;                         b0 = (f32x4){__uint_as_float(b4.x << 16), __uint_as_float(b4.x & 0xFFFF0000u), __uint_as_float(b4.y << 16), __uint_as_float(b4.y & 0xFFFF0000u)};
;                         b1 = (f32x4){__uint_as_float(b4.z << 16), __uint_as_float(b4.z & 0xFFFF0000u), __uint_as_float(b4.w << 16), __uint_as_float(b4.w & 0xFFFF0000u)}; }
;                     const f32x4 o0 = b0 + acc[ai][bj][m][0], o1 = b1 + acc[ai][bj][m][1];
.LBB0_1864:
	v_lshlrev_b64 v[194:195], 10, v[220:221]
	v_lshl_add_u64 v[224:225], v[194:195], 0, v[218:219]
	v_cndmask_b32_e64 v194, 0, 1, s[18:19]
	s_mov_b64 s[34:35], -1
	v_cmp_ne_u32_e64 s[8:9], 1, v194
	s_andn2_b64 vcc, exec, s[18:19]
	v_lshl_add_u64 v[222:223], v[224:225], 2, s[10:11]
	s_cbranch_vccnz .LBB0_1866
	global_load_dwordx4 v[198:201], v[222:223], off offset:16 nt
	global_load_dwordx4 v[194:197], v[222:223], off nt
	global_load_dwordx4 v[244:247], v[222:223], off offset:528 nt
	global_load_dwordx4 v[248:251], v[222:223], off offset:512 nt
	s_mov_b64 s[34:35], 0

; __device__ __forceinline__ void st16_wt(void* p, u32x4 v) { asm volatile("global_store_dwordx4 %0, %1, off sc1\n\ts_nop 1" :: "v"(p), "v"(v) : "memory"); }
; __device__ __forceinline__ unsigned cvt_pk_bf16(float lo, float hi) { unsigned r; asm volatile("v_cvt_pk_bf16_f32 %0, %1, %2" : "=v"(r) : "v"(lo), "v"(hi)); return r; }
;     __device__ __forceinline__ void operator()(const Acc& acc, const Unit& u, int wr, int wc, int fr, int fq, const LAS float* tab) const {
;     ...
;                 for (int bj = 0; bj < 2; ++bj) { f32x4 b0, b1;
;                     if (base32) { b0 = __builtin_nontemporal_load((const f32x4*)(base32 + off + bj * HALF)); b1 = __builtin_nontemporal_load((const f32x4*)(base32 + off + bj * HALF + 4)); }
;                     else { const u32x4 b4 = rb[ai][m][bj];
;                         b0 = (f32x4){__uint_as_float(b4.x << 16), __uint_as_float(b4.x & 0xFFFF0000u), __uint_as_float(b4.y << 16), __uint_as_float(b4.y & 0xFFFF0000u)};
;                         b1 = (f32x4){__uint_as_float(b4.z << 16), __uint_as_float(b4.z & 0xFFFF0000u), __uint_as_float(b4.w << 16), __uint_as_float(b4.w & 0xFFFF0000u)}; }
;                     const f32x4 o0 = b0 + acc[ai][bj][m][0], o1 = b1 + acc[ai][bj][m][1];
;                     if (out32) {
;                         if (!dry) { *(f32x4*)(out32 + off + bj * HALF) = o0; *(f32x4*)(out32 + off + bj * HALF + 4) = o1; }
;                         continue; }
;                     ss += ((o0[0] * o0[0] + o0[1] * o0[1]) + (o0[2] * o0[2] + o0[3] * o0[3])) + ((o1[0] * o1[0] + o1[1] * o1[1]) + (o1[2] * o1[2] + o1[3] * o1[3]));
;                     u32x4 w; w.x = cvt_pk_bf16(o0[0], o0[1]); w.y = cvt_pk_bf16(o0[2], o0[3]); w.z = cvt_pk_bf16(o1[0], o1[1]); w.w = cvt_pk_bf16(o1[2], o1[3]);
;                     if (!dry) st16_wt(xb + off + bj * HALF, w); }
.LBB0_1868:
	v_lshl_add_u64 v[190:191], v[224:225], 1, s[14:15]
	s_waitcnt vmcnt(0)
	v_pk_add_f32 v[192:193], v[164:165], v[196:197]
	v_pk_add_f32 v[196:197], v[162:163], v[194:195]
	v_pk_add_f32 v[194:195], v[160:161], v[200:201]
	v_pk_add_f32 v[198:199], v[158:159], v[198:199]
	v_cvt_pk_bf16_f32 v158, v196, v197
	v_cvt_pk_bf16_f32 v159, v192, v193
	s_and_b64 vcc, exec, s[8:9]
	v_cvt_pk_bf16_f32 v160, v198, v199
	v_cvt_pk_bf16_f32 v161, v194, v195
	s_mov_b64 s[34:35], -1
	global_store_dwordx4 v[190:191], v[158:161], off sc1
	s_nop 1
	s_cbranch_vccnz .LBB0_1870
	s_nop 1
	v_mov_b32_e32 v162, v244
	v_mov_b32_e32 v163, v245
	v_mov_b32_e32 v164, v246
	v_mov_b32_e32 v165, v247
	v_mov_b32_e32 v158, v248
	v_mov_b32_e32 v159, v249
	v_mov_b32_e32 v160, v250
	v_mov_b32_e32 v161, v251
	s_mov_b64 s[34:35], 0

;     __device__ __forceinline__ void operator()(const Acc& acc, const Unit& u, int wr, int wc, int fr, int fq, const LAS float* tab) const {
;     ...
;                 const size_t row = (size_t)u.pm * BM + ai * HALF + wr * 64 + m * 16 + fr; const size_t off = row * D + col0; float ss = 0.f;
; #pragma unroll
;                 for (int bj = 0; bj < 2; ++bj) { f32x4 b0, b1;
;                     if (base32) { b0 = __builtin_nontemporal_load((const f32x4*)(base32 + off + bj * HALF)); b1 = __builtin_nontemporal_load((const f32x4*)(base32 + off + bj * HALF + 4)); }
;                     else { const u32x4 b4 = rb[ai][m][bj];
;                         b0 = (f32x4){__uint_as_float(b4.x << 16), __uint_as_float(b4.x & 0xFFFF0000u), __uint_as_float(b4.y << 16), __uint_as_float(b4.y & 0xFFFF0000u)};
;                         b1 = (f32x4){__uint_as_float(b4.z << 16), __uint_as_float(b4.z & 0xFFFF0000u), __uint_as_float(b4.w << 16), __uint_as_float(b4.w & 0xFFFF0000u)}; }
;                     const f32x4 o0 = b0 + acc[ai][bj][m][0], o1 = b1 + acc[ai][bj][m][1];
.LBB0_1874:
	s_or_b64 exec, exec, s[34:35]
	v_or_b32_e32 v158, 16, v220
	v_mov_b32_e32 v159, v221
	v_lshlrev_b64 v[146:147], 10, v[158:159]
	v_lshl_add_u64 v[160:161], v[146:147], 0, v[218:219]
	s_mov_b64 s[34:35], -1
	s_and_b64 vcc, exec, s[8:9]
	v_lshl_add_u64 v[162:163], v[160:161], 2, s[10:11]
	s_cbranch_vccnz .LBB0_1876
	global_load_dwordx4 v[150:153], v[162:163], off offset:16 nt
	global_load_dwordx4 v[146:149], v[162:163], off nt
	global_load_dwordx4 v[244:247], v[162:163], off offset:528 nt
	global_load_dwordx4 v[248:251], v[162:163], off offset:512 nt
	s_mov_b64 s[34:35], 0

; __device__ __forceinline__ void st16_wt(void* p, u32x4 v) { asm volatile("global_store_dwordx4 %0, %1, off sc1\n\ts_nop 1" :: "v"(p), "v"(v) : "memory"); }
; __device__ __forceinline__ unsigned cvt_pk_bf16(float lo, float hi) { unsigned r; asm volatile("v_cvt_pk_bf16_f32 %0, %1, %2" : "=v"(r) : "v"(lo), "v"(hi)); return r; }
;     __device__ __forceinline__ void operator()(const Acc& acc, const Unit& u, int wr, int wc, int fr, int fq, const LAS float* tab) const {
;     ...
;                 for (int bj = 0; bj < 2; ++bj) { f32x4 b0, b1;
;                     if (base32) { b0 = __builtin_nontemporal_load((const f32x4*)(base32 + off + bj * HALF)); b1 = __builtin_nontemporal_load((const f32x4*)(base32 + off + bj * HALF + 4)); }
;                     else { const u32x4 b4 = rb[ai][m][bj];
;                         b0 = (f32x4){__uint_as_float(b4.x << 16), __uint_as_float(b4.x & 0xFFFF0000u), __uint_as_float(b4.y << 16), __uint_as_float(b4.y & 0xFFFF0000u)};
;                         b1 = (f32x4){__uint_as_float(b4.z << 16), __uint_as_float(b4.z & 0xFFFF0000u), __uint_as_float(b4.w << 16), __uint_as_float(b4.w & 0xFFFF0000u)}; }
;                     const f32x4 o0 = b0 + acc[ai][bj][m][0], o1 = b1 + acc[ai][bj][m][1];
;                     if (out32) {
;                         if (!dry) { *(f32x4*)(out32 + off + bj * HALF) = o0; *(f32x4*)(out32 + off + bj * HALF + 4) = o1; }
;                         continue; }
;                     ss += ((o0[0] * o0[0] + o0[1] * o0[1]) + (o0[2] * o0[2] + o0[3] * o0[3])) + ((o1[0] * o1[0] + o1[1] * o1[1]) + (o1[2] * o1[2] + o1[3] * o1[3]));
;                     u32x4 w; w.x = cvt_pk_bf16(o0[0], o0[1]); w.y = cvt_pk_bf16(o0[2], o0[3]); w.z = cvt_pk_bf16(o1[0], o1[1]); w.w = cvt_pk_bf16(o1[2], o1[3]);
;                     if (!dry) st16_wt(xb + off + bj * HALF, w); }
.LBB0_1878:
	v_lshl_add_u64 v[160:161], v[160:161], 1, s[14:15]
	s_waitcnt vmcnt(0)
	v_pk_add_f32 v[148:149], v[136:137], v[148:149]
	v_pk_add_f32 v[164:165], v[134:135], v[146:147]
	v_pk_add_f32 v[146:147], v[132:133], v[152:153]
	v_pk_add_f32 v[150:151], v[130:131], v[150:151]
	v_cvt_pk_bf16_f32 v130, v164, v165
	v_cvt_pk_bf16_f32 v131, v148, v149
	s_and_b64 vcc, exec, s[8:9]
	v_cvt_pk_bf16_f32 v132, v150, v151
	v_cvt_pk_bf16_f32 v133, v146, v147
	s_mov_b64 s[34:35], -1
	global_store_dwordx4 v[160:161], v[130:133], off sc1
	s_nop 1
	s_cbranch_vccnz .LBB0_1880
	s_nop 1
	v_mov_b32_e32 v134, v244
	v_mov_b32_e32 v135, v245
	v_mov_b32_e32 v136, v246
	v_mov_b32_e32 v137, v247
	v_mov_b32_e32 v130, v248
	v_mov_b32_e32 v131, v249
	v_mov_b32_e32 v132, v250
	v_mov_b32_e32 v133, v251
	s_mov_b64 s[34:35], 0

;     __device__ __forceinline__ void operator()(const Acc& acc, const Unit& u, int wr, int wc, int fr, int fq, const LAS float* tab) const {
;     ...
;                 const size_t row = (size_t)u.pm * BM + ai * HALF + wr * 64 + m * 16 + fr; const size_t off = row * D + col0; float ss = 0.f;
; #pragma unroll
;                 for (int bj = 0; bj < 2; ++bj) { f32x4 b0, b1;
;                     if (base32) { b0 = __builtin_nontemporal_load((const f32x4*)(base32 + off + bj * HALF)); b1 = __builtin_nontemporal_load((const f32x4*)(base32 + off + bj * HALF + 4)); }
;                     else { const u32x4 b4 = rb[ai][m][bj];
;                         b0 = (f32x4){__uint_as_float(b4.x << 16), __uint_as_float(b4.x & 0xFFFF0000u), __uint_as_float(b4.y << 16), __uint_as_float(b4.y & 0xFFFF0000u)};
;                         b1 = (f32x4){__uint_as_float(b4.z << 16), __uint_as_float(b4.z & 0xFFFF0000u), __uint_as_float(b4.w << 16), __uint_as_float(b4.w & 0xFFFF0000u)}; }
;                     const f32x4 o0 = b0 + acc[ai][bj][m][0], o1 = b1 + acc[ai][bj][m][1];
.LBB0_1884:
	s_or_b64 exec, exec, s[34:35]
	v_or_b32_e32 v130, 32, v220
	v_mov_b32_e32 v131, v221
	v_lshlrev_b64 v[118:119], 10, v[130:131]
	v_lshl_add_u64 v[132:133], v[118:119], 0, v[218:219]
	s_mov_b64 s[34:35], -1
	s_and_b64 vcc, exec, s[8:9]
	v_lshl_add_u64 v[134:135], v[132:133], 2, s[10:11]
	s_cbranch_vccnz .LBB0_1886
	global_load_dwordx4 v[126:129], v[134:135], off offset:16 nt
	global_load_dwordx4 v[118:121], v[134:135], off nt
	global_load_dwordx4 v[244:247], v[134:135], off offset:528 nt
	global_load_dwordx4 v[248:251], v[134:135], off offset:512 nt
	s_mov_b64 s[34:35], 0

; __device__ __forceinline__ void st16_wt(void* p, u32x4 v) { asm volatile("global_store_dwordx4 %0, %1, off sc1\n\ts_nop 1" :: "v"(p), "v"(v) : "memory"); }
; __device__ __forceinline__ unsigned cvt_pk_bf16(float lo, float hi) { unsigned r; asm volatile("v_cvt_pk_bf16_f32 %0, %1, %2" : "=v"(r) : "v"(lo), "v"(hi)); return r; }
;     __device__ __forceinline__ void operator()(const Acc& acc, const Unit& u, int wr, int wc, int fr, int fq, const LAS float* tab) const {
;     ...
;                 for (int bj = 0; bj < 2; ++bj) { f32x4 b0, b1;
;                     if (base32) { b0 = __builtin_nontemporal_load((const f32x4*)(base32 + off + bj * HALF)); b1 = __builtin_nontemporal_load((const f32x4*)(base32 + off + bj * HALF + 4)); }
;                     else { const u32x4 b4 = rb[ai][m][bj];
;                         b0 = (f32x4){__uint_as_float(b4.x << 16), __uint_as_float(b4.x & 0xFFFF0000u), __uint_as_float(b4.y << 16), __uint_as_float(b4.y & 0xFFFF0000u)};
;                         b1 = (f32x4){__uint_as_float(b4.z << 16), __uint_as_float(b4.z & 0xFFFF0000u), __uint_as_float(b4.w << 16), __uint_as_float(b4.w & 0xFFFF0000u)}; }
;                     const f32x4 o0 = b0 + acc[ai][bj][m][0], o1 = b1 + acc[ai][bj][m][1];
;                     if (out32) {
;                         if (!dry) { *(f32x4*)(out32 + off + bj * HALF) = o0; *(f32x4*)(out32 + off + bj * HALF + 4) = o1; }
;                         continue; }
;                     ss += ((o0[0] * o0[0] + o0[1] * o0[1]) + (o0[2] * o0[2] + o0[3] * o0[3])) + ((o1[0] * o1[0] + o1[1] * o1[1]) + (o1[2] * o1[2] + o1[3] * o1[3]));
;                     u32x4 w; w.x = cvt_pk_bf16(o0[0], o0[1]); w.y = cvt_pk_bf16(o0[2], o0[3]); w.z = cvt_pk_bf16(o1[0], o1[1]); w.w = cvt_pk_bf16(o1[2], o1[3]);
;                     if (!dry) st16_wt(xb + off + bj * HALF, w); }
.LBB0_1888:
	v_lshl_add_u64 v[132:133], v[132:133], 1, s[14:15]
	s_waitcnt vmcnt(0)
	v_pk_add_f32 v[120:121], v[112:113], v[120:121]
	v_pk_add_f32 v[136:137], v[110:111], v[118:119]
	v_pk_add_f32 v[118:119], v[108:109], v[128:129]
	v_pk_add_f32 v[126:127], v[106:107], v[126:127]
	v_cvt_pk_bf16_f32 v106, v136, v137
	v_cvt_pk_bf16_f32 v107, v120, v121
	s_and_b64 vcc, exec, s[8:9]
	v_cvt_pk_bf16_f32 v108, v126, v127
	v_cvt_pk_bf16_f32 v109, v118, v119
	s_mov_b64 s[34:35], -1
	global_store_dwordx4 v[132:133], v[106:109], off sc1
	s_nop 1
	s_cbranch_vccnz .LBB0_1890
	s_nop 1
	v_mov_b32_e32 v110, v244
	v_mov_b32_e32 v111, v245
	v_mov_b32_e32 v112, v246
	v_mov_b32_e32 v113, v247
	v_mov_b32_e32 v106, v248
	v_mov_b32_e32 v107, v249
	v_mov_b32_e32 v108, v250
	v_mov_b32_e32 v109, v251
	s_mov_b64 s[34:35], 0

;     __device__ __forceinline__ void operator()(const Acc& acc, const Unit& u, int wr, int wc, int fr, int fq, const LAS float* tab) const {
;     ...
;                 const size_t row = (size_t)u.pm * BM + ai * HALF + wr * 64 + m * 16 + fr; const size_t off = row * D + col0; float ss = 0.f;
; #pragma unroll
;                 for (int bj = 0; bj < 2; ++bj) { f32x4 b0, b1;
;                     if (base32) { b0 = __builtin_nontemporal_load((const f32x4*)(base32 + off + bj * HALF)); b1 = __builtin_nontemporal_load((const f32x4*)(base32 + off + bj * HALF + 4)); }
.LBB0_1894:
	s_or_b64 exec, exec, s[34:35]
	v_or_b32_e32 v106, 48, v220
	v_mov_b32_e32 v107, v221
	v_lshlrev_b64 v[94:95], 10, v[106:107]
	v_lshl_add_u64 v[108:109], v[94:95], 0, v[218:219]
	s_mov_b64 s[34:35], -1
	s_and_b64 vcc, exec, s[8:9]
	v_lshl_add_u64 v[110:111], v[108:109], 2, s[10:11]
	s_cbranch_vccnz .LBB0_1896
	global_load_dwordx4 v[98:101], v[110:111], off offset:16 nt
	global_load_dwordx4 v[94:97], v[110:111], off nt
	global_load_dwordx4 v[244:247], v[110:111], off offset:528 nt
	global_load_dwordx4 v[248:251], v[110:111], off offset:512 nt
	s_mov_b64 s[34:35], 0

; __device__ __forceinline__ void st16_wt(void* p, u32x4 v) { asm volatile("global_store_dwordx4 %0, %1, off sc1\n\ts_nop 1" :: "v"(p), "v"(v) : "memory"); }
; __device__ __forceinline__ unsigned cvt_pk_bf16(float lo, float hi) { unsigned r; asm volatile("v_cvt_pk_bf16_f32 %0, %1, %2" : "=v"(r) : "v"(lo), "v"(hi)); return r; }
;     __device__ __forceinline__ void operator()(const Acc& acc, const Unit& u, int wr, int wc, int fr, int fq, const LAS float* tab) const {
;     ...
;                 for (int bj = 0; bj < 2; ++bj) { f32x4 b0, b1;
;                     if (base32) { b0 = __builtin_nontemporal_load((const f32x4*)(base32 + off + bj * HALF)); b1 = __builtin_nontemporal_load((const f32x4*)(base32 + off + bj * HALF + 4)); }
;                     else { const u32x4 b4 = rb[ai][m][bj];
;                         b0 = (f32x4){__uint_as_float(b4.x << 16), __uint_as_float(b4.x & 0xFFFF0000u), __uint_as_float(b4.y << 16), __uint_as_float(b4.y & 0xFFFF0000u)};
;                         b1 = (f32x4){__uint_as_float(b4.z << 16), __uint_as_float(b4.z & 0xFFFF0000u), __uint_as_float(b4.w << 16), __uint_as_float(b4.w & 0xFFFF0000u)}; }
;                     const f32x4 o0 = b0 + acc[ai][bj][m][0], o1 = b1 + acc[ai][bj][m][1];
;                     if (out32) {
;                         if (!dry) { *(f32x4*)(out32 + off + bj * HALF) = o0; *(f32x4*)(out32 + off + bj * HALF + 4) = o1; }
;                         continue; }
;                     ss += ((o0[0] * o0[0] + o0[1] * o0[1]) + (o0[2] * o0[2] + o0[3] * o0[3])) + ((o1[0] * o1[0] + o1[1] * o1[1]) + (o1[2] * o1[2] + o1[3] * o1[3]));
;                     u32x4 w; w.x = cvt_pk_bf16(o0[0], o0[1]); w.y = cvt_pk_bf16(o0[2], o0[3]); w.z = cvt_pk_bf16(o1[0], o1[1]); w.w = cvt_pk_bf16(o1[2], o1[3]);
;                     if (!dry) st16_wt(xb + off + bj * HALF, w); }
.LBB0_1898:
	v_lshl_add_u64 v[108:109], v[108:109], 1, s[14:15]
	s_waitcnt vmcnt(0)
	v_pk_add_f32 v[96:97], v[88:89], v[96:97]
	v_pk_add_f32 v[112:113], v[86:87], v[94:95]
	v_pk_add_f32 v[94:95], v[84:85], v[100:101]
	v_pk_add_f32 v[98:99], v[82:83], v[98:99]
	v_cvt_pk_bf16_f32 v82, v112, v113
	v_cvt_pk_bf16_f32 v83, v96, v97
	s_and_b64 vcc, exec, s[8:9]
	v_cvt_pk_bf16_f32 v84, v98, v99
	v_cvt_pk_bf16_f32 v85, v94, v95
	s_mov_b64 s[34:35], -1
	global_store_dwordx4 v[108:109], v[82:85], off sc1
	s_nop 1
	s_cbranch_vccnz .LBB0_1900
	s_nop 1
	v_mov_b32_e32 v86, v244
	v_mov_b32_e32 v87, v245
	v_mov_b32_e32 v88, v246
	v_mov_b32_e32 v89, v247
	v_mov_b32_e32 v82, v248
	v_mov_b32_e32 v83, v249
	v_mov_b32_e32 v84, v250
	v_mov_b32_e32 v85, v251
	s_mov_b64 s[34:35], 0

;     __device__ __forceinline__ void operator()(const Acc& acc, const Unit& u, int wr, int wc, int fr, int fq, const LAS float* tab) const {
;     ...
;                 const size_t row = (size_t)u.pm * BM + ai * HALF + wr * 64 + m * 16 + fr; const size_t off = row * D + col0; float ss = 0.f;
; #pragma unroll
;                 for (int bj = 0; bj < 2; ++bj) { f32x4 b0, b1;
;                     if (base32) { b0 = __builtin_nontemporal_load((const f32x4*)(base32 + off + bj * HALF)); b1 = __builtin_nontemporal_load((const f32x4*)(base32 + off + bj * HALF + 4)); }
.LBB0_1904:
	s_or_b64 exec, exec, s[34:35]
	v_lshl_add_u64 v[82:83], v[220:221], 0, s[90:91]
	v_lshlrev_b64 v[70:71], 10, v[82:83]
	v_lshl_add_u64 v[84:85], v[70:71], 0, v[218:219]
	s_mov_b64 s[34:35], -1
	s_and_b64 vcc, exec, s[8:9]
	v_lshl_add_u64 v[86:87], v[84:85], 2, s[10:11]
	s_cbranch_vccnz .LBB0_1906
	global_load_dwordx4 v[74:77], v[86:87], off offset:16 nt
	global_load_dwordx4 v[70:73], v[86:87], off nt
	global_load_dwordx4 v[244:247], v[86:87], off offset:528 nt
	global_load_dwordx4 v[248:251], v[86:87], off offset:512 nt
	s_mov_b64 s[34:35], 0

; __device__ __forceinline__ void st16_wt(void* p, u32x4 v) { asm volatile("global_store_dwordx4 %0, %1, off sc1\n\ts_nop 1" :: "v"(p), "v"(v) : "memory"); }
; __device__ __forceinline__ unsigned cvt_pk_bf16(float lo, float hi) { unsigned r; asm volatile("v_cvt_pk_bf16_f32 %0, %1, %2" : "=v"(r) : "v"(lo), "v"(hi)); return r; }
;     __device__ __forceinline__ void operator()(const Acc& acc, const Unit& u, int wr, int wc, int fr, int fq, const LAS float* tab) const {
;     ...
;                 for (int bj = 0; bj < 2; ++bj) { f32x4 b0, b1;
;                     if (base32) { b0 = __builtin_nontemporal_load((const f32x4*)(base32 + off + bj * HALF)); b1 = __builtin_nontemporal_load((const f32x4*)(base32 + off + bj * HALF + 4)); }
;                     else { const u32x4 b4 = rb[ai][m][bj];
;                         b0 = (f32x4){__uint_as_float(b4.x << 16), __uint_as_float(b4.x & 0xFFFF0000u), __uint_as_float(b4.y << 16), __uint_as_float(b4.y & 0xFFFF0000u)};
;                         b1 = (f32x4){__uint_as_float(b4.z << 16), __uint_as_float(b4.z & 0xFFFF0000u), __uint_as_float(b4.w << 16), __uint_as_float(b4.w & 0xFFFF0000u)}; }
;                     const f32x4 o0 = b0 + acc[ai][bj][m][0], o1 = b1 + acc[ai][bj][m][1];
;                     if (out32) {
;                         if (!dry) { *(f32x4*)(out32 + off + bj * HALF) = o0; *(f32x4*)(out32 + off + bj * HALF + 4) = o1; }
;                         continue; }
;                     ss += ((o0[0] * o0[0] + o0[1] * o0[1]) + (o0[2] * o0[2] + o0[3] * o0[3])) + ((o1[0] * o1[0] + o1[1] * o1[1]) + (o1[2] * o1[2] + o1[3] * o1[3]));
;                     u32x4 w; w.x = cvt_pk_bf16(o0[0], o0[1]); w.y = cvt_pk_bf16(o0[2], o0[3]); w.z = cvt_pk_bf16(o1[0], o1[1]); w.w = cvt_pk_bf16(o1[2], o1[3]);
;                     if (!dry) st16_wt(xb + off + bj * HALF, w); }
.LBB0_1908:
	v_lshl_add_u64 v[84:85], v[84:85], 1, s[14:15]
	s_waitcnt vmcnt(0)
	v_pk_add_f32 v[72:73], v[64:65], v[72:73]
	v_pk_add_f32 v[88:89], v[62:63], v[70:71]
	v_pk_add_f32 v[70:71], v[60:61], v[76:77]
	v_pk_add_f32 v[74:75], v[58:59], v[74:75]
	v_cvt_pk_bf16_f32 v58, v88, v89
	v_cvt_pk_bf16_f32 v59, v72, v73
	s_and_b64 vcc, exec, s[8:9]
	v_cvt_pk_bf16_f32 v60, v74, v75
	v_cvt_pk_bf16_f32 v61, v70, v71
	s_mov_b64 s[34:35], -1
	global_store_dwordx4 v[84:85], v[58:61], off sc1
	s_nop 1
	s_cbranch_vccnz .LBB0_1910
	s_nop 1
	v_mov_b32_e32 v62, v244
	v_mov_b32_e32 v63, v245
	v_mov_b32_e32 v64, v246
	v_mov_b32_e32 v65, v247
	v_mov_b32_e32 v58, v248
	v_mov_b32_e32 v59, v249
	v_mov_b32_e32 v60, v250
	v_mov_b32_e32 v61, v251
	s_mov_b64 s[34:35], 0

;     __device__ __forceinline__ void operator()(const Acc& acc, const Unit& u, int wr, int wc, int fr, int fq, const LAS float* tab) const {
;     ...
;                 const size_t row = (size_t)u.pm * BM + ai * HALF + wr * 64 + m * 16 + fr; const size_t off = row * D + col0; float ss = 0.f;
; #pragma unroll
;                 for (int bj = 0; bj < 2; ++bj) { f32x4 b0, b1;
;                     if (base32) { b0 = __builtin_nontemporal_load((const f32x4*)(base32 + off + bj * HALF)); b1 = __builtin_nontemporal_load((const f32x4*)(base32 + off + bj * HALF + 4)); }
.LBB0_1914:
	s_or_b64 exec, exec, s[34:35]
	s_mov_b64 s[0:1], 0x90
	v_lshl_add_u64 v[58:59], v[220:221], 0, s[0:1]
	v_lshlrev_b64 v[50:51], 10, v[58:59]
	v_lshl_add_u64 v[60:61], v[50:51], 0, v[218:219]
	s_mov_b64 s[34:35], -1
	s_and_b64 vcc, exec, s[8:9]
	v_lshl_add_u64 v[62:63], v[60:61], 2, s[10:11]
	s_cbranch_vccnz .LBB0_1916
	global_load_dwordx4 v[54:57], v[62:63], off offset:16 nt
	global_load_dwordx4 v[50:53], v[62:63], off nt
	global_load_dwordx4 v[244:247], v[62:63], off offset:528 nt
	global_load_dwordx4 v[248:251], v[62:63], off offset:512 nt
	s_mov_b64 s[34:35], 0

; __device__ __forceinline__ void st16_wt(void* p, u32x4 v) { asm volatile("global_store_dwordx4 %0, %1, off sc1\n\ts_nop 1" :: "v"(p), "v"(v) : "memory"); }
; __device__ __forceinline__ unsigned cvt_pk_bf16(float lo, float hi) { unsigned r; asm volatile("v_cvt_pk_bf16_f32 %0, %1, %2" : "=v"(r) : "v"(lo), "v"(hi)); return r; }
;     __device__ __forceinline__ void operator()(const Acc& acc, const Unit& u, int wr, int wc, int fr, int fq, const LAS float* tab) const {
;     ...
;                 for (int bj = 0; bj < 2; ++bj) { f32x4 b0, b1;
;                     if (base32) { b0 = __builtin_nontemporal_load((const f32x4*)(base32 + off + bj * HALF)); b1 = __builtin_nontemporal_load((const f32x4*)(base32 + off + bj * HALF + 4)); }
;                     else { const u32x4 b4 = rb[ai][m][bj];
;                         b0 = (f32x4){__uint_as_float(b4.x << 16), __uint_as_float(b4.x & 0xFFFF0000u), __uint_as_float(b4.y << 16), __uint_as_float(b4.y & 0xFFFF0000u)};
;                         b1 = (f32x4){__uint_as_float(b4.z << 16), __uint_as_float(b4.z & 0xFFFF0000u), __uint_as_float(b4.w << 16), __uint_as_float(b4.w & 0xFFFF0000u)}; }
;                     const f32x4 o0 = b0 + acc[ai][bj][m][0], o1 = b1 + acc[ai][bj][m][1];
;                     if (out32) {
;                         if (!dry) { *(f32x4*)(out32 + off + bj * HALF) = o0; *(f32x4*)(out32 + off + bj * HALF + 4) = o1; }
;                         continue; }
;                     ss += ((o0[0] * o0[0] + o0[1] * o0[1]) + (o0[2] * o0[2] + o0[3] * o0[3])) + ((o1[0] * o1[0] + o1[1] * o1[1]) + (o1[2] * o1[2] + o1[3] * o1[3]));
;                     u32x4 w; w.x = cvt_pk_bf16(o0[0], o0[1]); w.y = cvt_pk_bf16(o0[2], o0[3]); w.z = cvt_pk_bf16(o1[0], o1[1]); w.w = cvt_pk_bf16(o1[2], o1[3]);
;                     if (!dry) st16_wt(xb + off + bj * HALF, w); }
.LBB0_1918:
	v_lshl_add_u64 v[60:61], v[60:61], 1, s[14:15]
	s_waitcnt vmcnt(0)
	v_pk_add_f32 v[52:53], v[48:49], v[52:53]
	v_pk_add_f32 v[64:65], v[46:47], v[50:51]
	v_pk_add_f32 v[50:51], v[44:45], v[56:57]
	v_pk_add_f32 v[54:55], v[42:43], v[54:55]
	v_cvt_pk_bf16_f32 v42, v64, v65
	v_cvt_pk_bf16_f32 v43, v52, v53
	s_and_b64 vcc, exec, s[8:9]
	v_cvt_pk_bf16_f32 v44, v54, v55
	v_cvt_pk_bf16_f32 v45, v50, v51
	s_mov_b64 s[34:35], -1
	global_store_dwordx4 v[60:61], v[42:45], off sc1
	s_nop 1
	s_cbranch_vccnz .LBB0_1920
	s_nop 1
	v_mov_b32_e32 v46, v244
	v_mov_b32_e32 v47, v245
	v_mov_b32_e32 v48, v246
	v_mov_b32_e32 v49, v247
	v_mov_b32_e32 v42, v248
	v_mov_b32_e32 v43, v249
	v_mov_b32_e32 v44, v250
	v_mov_b32_e32 v45, v251
	s_mov_b64 s[34:35], 0

;     __device__ __forceinline__ void operator()(const Acc& acc, const Unit& u, int wr, int wc, int fr, int fq, const LAS float* tab) const {
;     ...
;                 const size_t row = (size_t)u.pm * BM + ai * HALF + wr * 64 + m * 16 + fr; const size_t off = row * D + col0; float ss = 0.f;
; #pragma unroll
;                 for (int bj = 0; bj < 2; ++bj) { f32x4 b0, b1;
;                     if (base32) { b0 = __builtin_nontemporal_load((const f32x4*)(base32 + off + bj * HALF)); b1 = __builtin_nontemporal_load((const f32x4*)(base32 + off + bj * HALF + 4)); }
.LBB0_1924:
	s_or_b64 exec, exec, s[34:35]
	s_mov_b64 s[0:1], 0xa0
	v_lshl_add_u64 v[42:43], v[220:221], 0, s[0:1]
	v_lshlrev_b64 v[34:35], 10, v[42:43]
	v_lshl_add_u64 v[44:45], v[34:35], 0, v[218:219]
	s_mov_b64 s[34:35], -1
	s_and_b64 vcc, exec, s[8:9]
	v_lshl_add_u64 v[46:47], v[44:45], 2, s[10:11]
	s_cbranch_vccnz .LBB0_1926
	global_load_dwordx4 v[38:41], v[46:47], off offset:16 nt
	global_load_dwordx4 v[34:37], v[46:47], off nt
	global_load_dwordx4 v[244:247], v[46:47], off offset:528 nt
	global_load_dwordx4 v[248:251], v[46:47], off offset:512 nt
	s_mov_b64 s[34:35], 0

; __device__ __forceinline__ void st16_wt(void* p, u32x4 v) { asm volatile("global_store_dwordx4 %0, %1, off sc1\n\ts_nop 1" :: "v"(p), "v"(v) : "memory"); }
; __device__ __forceinline__ unsigned cvt_pk_bf16(float lo, float hi) { unsigned r; asm volatile("v_cvt_pk_bf16_f32 %0, %1, %2" : "=v"(r) : "v"(lo), "v"(hi)); return r; }
;     __device__ __forceinline__ void operator()(const Acc& acc, const Unit& u, int wr, int wc, int fr, int fq, const LAS float* tab) const {
;     ...
;                 for (int bj = 0; bj < 2; ++bj) { f32x4 b0, b1;
;                     if (base32) { b0 = __builtin_nontemporal_load((const f32x4*)(base32 + off + bj * HALF)); b1 = __builtin_nontemporal_load((const f32x4*)(base32 + off + bj * HALF + 4)); }
;                     else { const u32x4 b4 = rb[ai][m][bj];
;                         b0 = (f32x4){__uint_as_float(b4.x << 16), __uint_as_float(b4.x & 0xFFFF0000u), __uint_as_float(b4.y << 16), __uint_as_float(b4.y & 0xFFFF0000u)};
;                         b1 = (f32x4){__uint_as_float(b4.z << 16), __uint_as_float(b4.z & 0xFFFF0000u), __uint_as_float(b4.w << 16), __uint_as_float(b4.w & 0xFFFF0000u)}; }
;                     const f32x4 o0 = b0 + acc[ai][bj][m][0], o1 = b1 + acc[ai][bj][m][1];
;                     if (out32) {
;                         if (!dry) { *(f32x4*)(out32 + off + bj * HALF) = o0; *(f32x4*)(out32 + off + bj * HALF + 4) = o1; }
;                         continue; }
;                     ss += ((o0[0] * o0[0] + o0[1] * o0[1]) + (o0[2] * o0[2] + o0[3] * o0[3])) + ((o1[0] * o1[0] + o1[1] * o1[1]) + (o1[2] * o1[2] + o1[3] * o1[3]));
;                     u32x4 w; w.x = cvt_pk_bf16(o0[0], o0[1]); w.y = cvt_pk_bf16(o0[2], o0[3]); w.z = cvt_pk_bf16(o1[0], o1[1]); w.w = cvt_pk_bf16(o1[2], o1[3]);
;                     if (!dry) st16_wt(xb + off + bj * HALF, w); }
.LBB0_1928:
	v_lshl_add_u64 v[44:45], v[44:45], 1, s[14:15]
	s_waitcnt vmcnt(0)
	v_pk_add_f32 v[36:37], v[32:33], v[36:37]
	v_pk_add_f32 v[48:49], v[30:31], v[34:35]
	v_pk_add_f32 v[34:35], v[28:29], v[40:41]
	v_pk_add_f32 v[38:39], v[26:27], v[38:39]
	v_cvt_pk_bf16_f32 v26, v48, v49
	v_cvt_pk_bf16_f32 v27, v36, v37
	s_and_b64 vcc, exec, s[8:9]
	v_cvt_pk_bf16_f32 v28, v38, v39
	v_cvt_pk_bf16_f32 v29, v34, v35
	s_mov_b64 s[34:35], -1
	global_store_dwordx4 v[44:45], v[26:29], off sc1
	s_nop 1
	s_cbranch_vccnz .LBB0_1930
	s_nop 1
	v_mov_b32_e32 v30, v244
	v_mov_b32_e32 v31, v245
	v_mov_b32_e32 v32, v246
	v_mov_b32_e32 v33, v247
	v_mov_b32_e32 v26, v248
	v_mov_b32_e32 v27, v249
	v_mov_b32_e32 v28, v250
	v_mov_b32_e32 v29, v251
	s_mov_b64 s[34:35], 0

;     __device__ __forceinline__ void operator()(const Acc& acc, const Unit& u, int wr, int wc, int fr, int fq, const LAS float* tab) const {
;     ...
;                 const size_t row = (size_t)u.pm * BM + ai * HALF + wr * 64 + m * 16 + fr; const size_t off = row * D + col0; float ss = 0.f;
; #pragma unroll
;                 for (int bj = 0; bj < 2; ++bj) { f32x4 b0, b1;
;                     if (base32) { b0 = __builtin_nontemporal_load((const f32x4*)(base32 + off + bj * HALF)); b1 = __builtin_nontemporal_load((const f32x4*)(base32 + off + bj * HALF + 4)); }
.LBB0_1934:
	s_or_b64 exec, exec, s[34:35]
	s_mov_b64 s[0:1], 0xb0
	v_lshl_add_u64 v[26:27], v[220:221], 0, s[0:1]
	v_lshlrev_b64 v[18:19], 10, v[26:27]
	v_lshl_add_u64 v[28:29], v[18:19], 0, v[218:219]
	s_mov_b64 s[34:35], -1
	s_and_b64 vcc, exec, s[8:9]
	v_lshl_add_u64 v[30:31], v[28:29], 2, s[10:11]
	s_cbranch_vccnz .LBB0_1936
	global_load_dwordx4 v[22:25], v[30:31], off offset:16 nt
	global_load_dwordx4 v[18:21], v[30:31], off nt
	global_load_dwordx4 v[244:247], v[30:31], off offset:528 nt
	global_load_dwordx4 v[248:251], v[30:31], off offset:512 nt
	s_mov_b64 s[34:35], 0

; __device__ __forceinline__ void st16_wt(void* p, u32x4 v) { asm volatile("global_store_dwordx4 %0, %1, off sc1\n\ts_nop 1" :: "v"(p), "v"(v) : "memory"); }
; __device__ __forceinline__ unsigned cvt_pk_bf16(float lo, float hi) { unsigned r; asm volatile("v_cvt_pk_bf16_f32 %0, %1, %2" : "=v"(r) : "v"(lo), "v"(hi)); return r; }
;     __device__ __forceinline__ void operator()(const Acc& acc, const Unit& u, int wr, int wc, int fr, int fq, const LAS float* tab) const {
;     ...
;                 for (int bj = 0; bj < 2; ++bj) { f32x4 b0, b1;
;                     if (base32) { b0 = __builtin_nontemporal_load((const f32x4*)(base32 + off + bj * HALF)); b1 = __builtin_nontemporal_load((const f32x4*)(base32 + off + bj * HALF + 4)); }
;                     else { const u32x4 b4 = rb[ai][m][bj];
;                         b0 = (f32x4){__uint_as_float(b4.x << 16), __uint_as_float(b4.x & 0xFFFF0000u), __uint_as_float(b4.y << 16), __uint_as_float(b4.y & 0xFFFF0000u)};
;                         b1 = (f32x4){__uint_as_float(b4.z << 16), __uint_as_float(b4.z & 0xFFFF0000u), __uint_as_float(b4.w << 16), __uint_as_float(b4.w & 0xFFFF0000u)}; }
;                     const f32x4 o0 = b0 + acc[ai][bj][m][0], o1 = b1 + acc[ai][bj][m][1];
;                     if (out32) {
;                         if (!dry) { *(f32x4*)(out32 + off + bj * HALF) = o0; *(f32x4*)(out32 + off + bj * HALF + 4) = o1; }
;                         continue; }
;                     ss += ((o0[0] * o0[0] + o0[1] * o0[1]) + (o0[2] * o0[2] + o0[3] * o0[3])) + ((o1[0] * o1[0] + o1[1] * o1[1]) + (o1[2] * o1[2] + o1[3] * o1[3]));
;                     u32x4 w; w.x = cvt_pk_bf16(o0[0], o0[1]); w.y = cvt_pk_bf16(o0[2], o0[3]); w.z = cvt_pk_bf16(o1[0], o1[1]); w.w = cvt_pk_bf16(o1[2], o1[3]);
;                     if (!dry) st16_wt(xb + off + bj * HALF, w); }
.LBB0_1938:
	v_lshl_add_u64 v[28:29], v[28:29], 1, s[14:15]
	s_waitcnt vmcnt(0)
	v_pk_add_f32 v[20:21], v[16:17], v[20:21]
	v_pk_add_f32 v[32:33], v[14:15], v[18:19]
	v_pk_add_f32 v[18:19], v[12:13], v[24:25]
	v_pk_add_f32 v[22:23], v[10:11], v[22:23]
	v_cvt_pk_bf16_f32 v10, v32, v33
	v_cvt_pk_bf16_f32 v11, v20, v21
	s_and_b64 vcc, exec, s[8:9]
	v_cvt_pk_bf16_f32 v12, v22, v23
	v_cvt_pk_bf16_f32 v13, v18, v19
	s_mov_b64 s[8:9], -1
	global_store_dwordx4 v[28:29], v[10:13], off sc1
	s_nop 1
	s_cbranch_vccnz .LBB0_1940
	s_nop 1
	v_mov_b32_e32 v14, v244
	v_mov_b32_e32 v15, v245
	v_mov_b32_e32 v16, v246
	v_mov_b32_e32 v17, v247
	v_mov_b32_e32 v10, v248
	v_mov_b32_e32 v11, v249
	v_mov_b32_e32 v12, v250
	v_mov_b32_e32 v13, v251
	s_mov_b64 s[8:9], 0
